# expert-row conversion (both copies): first four butterfly steps of the two row reductions via DPP instead of ds_bpermute round trips (on top of v21)
# speedup vs baseline: 1.0043x; 1.0043x over previous
.Luv4_next_issued:
	s_or_b64 exec, exec, s[98:99]
	v_add_co_u32_e32 v34, vcc, s38, v2
	global_load_dwordx4 v[46:49], v[2:3], off
	global_load_dwordx4 v[30:33], v[2:3], off offset:1024
	global_load_dwordx4 v[26:29], v[2:3], off offset:2048
	global_load_dwordx4 v[18:21], v[2:3], off offset:3072
	v_addc_co_u32_e32 v35, vcc, 0, v3, vcc
	global_load_dwordx4 v[22:25], v[34:35], off offset:-4096
	v_add_co_u32_e32 v4, vcc, s36, v2
	s_waitcnt vmcnt(4)
	v_mul_f32_e32 v42, v47, v47
	v_addc_co_u32_e32 v5, vcc, 0, v3, vcc
	global_load_dwordx4 v[10:13], v[4:5], off offset:1024
	v_add_co_u32_e32 v36, vcc, s39, v2
	v_mul_f32_e32 v43, v49, v49
	s_nop 0
	v_addc_co_u32_e32 v37, vcc, 0, v3, vcc
	global_load_dwordx4 v[62:65], v[4:5], off offset:2048
	global_load_dwordx4 v[50:53], v[4:5], off offset:3072
	global_load_dwordx4 v[38:41], v[34:35], off
	global_load_dwordx4 v[14:17], v[34:35], off offset:1024
	global_load_dwordx4 v[6:9], v[34:35], off offset:2048
	s_nop 0
	global_load_dwordx4 v[2:5], v[36:37], off offset:3072
	v_max_f32_e64 v44, |v47|, |v47|
	v_max_f32_e64 v45, |v46|, |v46|
	v_max_f32_e64 v54, |v49|, |v49|
	v_max_f32_e64 v55, |v48|, |v48|
	s_waitcnt vmcnt(10)
	v_mul_f32_e32 v56, v31, v31
	v_mul_f32_e32 v57, v33, v33
	s_waitcnt vmcnt(9)
	v_mul_f32_e32 v69, v27, v27
	v_mul_f32_e32 v75, v29, v29
	v_fmac_f32_e32 v42, v46, v46
	v_fmac_f32_e32 v43, v48, v48
	v_max_f32_e32 v44, v45, v44
	v_max_f32_e32 v45, v55, v54
	v_fmac_f32_e32 v56, v30, v30
	v_fmac_f32_e32 v57, v32, v32
	v_max_f32_e64 v58, |v31|, |v31|
	v_max_f32_e64 v59, |v30|, |v30|
	v_max_f32_e64 v76, |v27|, |v27|
	v_max_f32_e64 v77, |v26|, |v26|
	s_waitcnt vmcnt(8)
	v_mul_f32_e32 v80, v19, v19
	v_mul_f32_e32 v81, v21, v21
	v_fmac_f32_e32 v69, v26, v26
	v_fmac_f32_e32 v75, v28, v28
	v_add_f32_e32 v42, v42, v43
	v_max3_f32 v43, v44, 0, v45
	v_add_f32_e32 v44, v56, v57
	v_max_f32_e32 v54, v59, v58
	v_max_f32_e32 v58, v77, v76
	v_fmac_f32_e32 v80, v18, v18
	v_fmac_f32_e32 v81, v20, v20
	s_waitcnt vmcnt(7)
	v_mul_f32_e32 v76, v23, v23
	v_mul_f32_e32 v77, v25, v25
	v_add_f32_e32 v45, v69, v75
	v_add_f32_e32 v42, v42, v44
	v_max_f32_e64 v60, |v33|, |v33|
	v_max_f32_e64 v61, |v32|, |v32|
	v_add_f32_e32 v56, v80, v81
	v_fmac_f32_e32 v76, v22, v22
	v_fmac_f32_e32 v77, v24, v24
	v_add_f32_e32 v42, v42, v45
	v_max_f32_e64 v78, |v29|, |v29|
	v_max_f32_e64 v79, |v28|, |v28|
	v_max_f32_e32 v55, v61, v60
	v_add_f32_e32 v42, v42, v56
	v_add_f32_e32 v44, v76, v77
	v_max_f32_e64 v82, |v19|, |v19|
	v_max_f32_e64 v83, |v18|, |v18|
	v_max_f32_e64 v84, |v21|, |v21|
	v_max_f32_e64 v85, |v20|, |v20|
	v_max_f32_e32 v59, v79, v78
	v_max3_f32 v43, v43, v54, v55
	v_add_f32_e32 v42, v42, v44
	v_max_f32_e64 v44, |v23|, |v23|
	v_max_f32_e64 v45, |v22|, |v22|
	v_max_f32_e32 v60, v83, v82
	v_max_f32_e32 v61, v85, v84
	v_max3_f32 v43, v43, v58, v59
	v_max_f32_e32 v44, v45, v44
	v_max_f32_e64 v45, |v25|, |v25|
	v_max_f32_e64 v54, |v24|, |v24|
	v_max3_f32 v43, v43, v60, v61
	v_max_f32_e32 v45, v54, v45
	v_max3_f32 v43, v43, v44, v45
	global_load_dwordx4 v[58:61], v[34:35], off offset:3072
	global_load_dwordx4 v[54:57], v[36:37], off
	v_cmp_lt_i32_e32 vcc, v157, v154
	s_waitcnt vmcnt(8)
	v_mul_f32_e32 v44, v11, v11
	v_mul_f32_e32 v34, v13, v13
	v_fmac_f32_e32 v44, v10, v10
	v_fmac_f32_e32 v34, v12, v12
	v_add_f32_e32 v34, v44, v34
	v_add_f32_e32 v34, v42, v34
	v_max_f32_e64 v35, |v11|, |v11|
	v_max_f32_e64 v42, |v10|, |v10|
	v_max_f32_e32 v35, v42, v35
	v_max_f32_e64 v42, |v13|, |v13|
	v_max_f32_e64 v44, |v12|, |v12|
	v_max_f32_e32 v42, v44, v42
	v_max3_f32 v35, v43, v35, v42
	s_waitcnt vmcnt(7)
	v_mul_f32_e32 v42, v63, v63
	v_mul_f32_e32 v43, v65, v65
	v_fmac_f32_e32 v42, v62, v62
	v_fmac_f32_e32 v43, v64, v64
	v_add_f32_e32 v42, v42, v43
	v_add_f32_e32 v34, v34, v42
	v_max_f32_e64 v42, |v63|, |v63|
	v_max_f32_e64 v43, |v62|, |v62|
	v_max_f32_e32 v42, v43, v42
	v_max_f32_e64 v43, |v65|, |v65|
	v_max_f32_e64 v44, |v64|, |v64|
	v_max_f32_e32 v43, v44, v43
	v_max3_f32 v69, v35, v42, v43
	global_load_dwordx4 v[42:45], v[36:37], off offset:1024
	s_waitcnt vmcnt(7)
	v_mul_f32_e32 v35, v51, v51
	v_mul_f32_e32 v75, v53, v53
	v_fmac_f32_e32 v35, v50, v50
	v_fmac_f32_e32 v75, v52, v52
	v_add_f32_e32 v35, v35, v75
	v_add_f32_e32 v75, v34, v35
	v_max_f32_e64 v34, |v51|, |v51|
	v_max_f32_e64 v35, |v50|, |v50|
	v_max_f32_e32 v76, v35, v34
	v_max_f32_e64 v34, |v53|, |v53|
	v_max_f32_e64 v35, |v52|, |v52|
	v_max_f32_e32 v77, v35, v34
	global_load_dwordx4 v[34:37], v[36:37], off offset:2048
	v_max3_f32 v69, v69, v76, v77
	s_waitcnt vmcnt(7)
	v_mul_f32_e32 v76, v39, v39
	v_mul_f32_e32 v77, v41, v41
	v_fmac_f32_e32 v76, v38, v38
	v_fmac_f32_e32 v77, v40, v40
	v_add_f32_e32 v76, v76, v77
	v_add_f32_e32 v75, v75, v76
	v_max_f32_e64 v76, |v39|, |v39|
	v_max_f32_e64 v77, |v38|, |v38|
	v_max_f32_e32 v76, v77, v76
	v_max_f32_e64 v77, |v41|, |v41|
	v_max_f32_e64 v78, |v40|, |v40|
	v_max_f32_e32 v77, v78, v77
	v_max3_f32 v69, v69, v76, v77
	s_waitcnt vmcnt(6)
	v_mul_f32_e32 v76, v15, v15
	v_mul_f32_e32 v77, v17, v17
	v_fmac_f32_e32 v76, v14, v14
	v_fmac_f32_e32 v77, v16, v16
	v_add_f32_e32 v76, v76, v77
	v_add_f32_e32 v75, v75, v76
	v_max_f32_e64 v76, |v15|, |v15|
	v_max_f32_e64 v77, |v14|, |v14|
	v_max_f32_e32 v76, v77, v76
	v_max_f32_e64 v77, |v17|, |v17|
	v_max_f32_e64 v78, |v16|, |v16|
	v_max_f32_e32 v77, v78, v77
	v_max3_f32 v69, v69, v76, v77
	s_waitcnt vmcnt(5)
	v_mul_f32_e32 v76, v7, v7
	v_mul_f32_e32 v77, v9, v9
	v_fmac_f32_e32 v76, v6, v6
	v_fmac_f32_e32 v77, v8, v8
	v_add_f32_e32 v76, v76, v77
	v_add_f32_e32 v75, v75, v76
	v_max_f32_e64 v76, |v7|, |v7|
	v_max_f32_e64 v77, |v6|, |v6|
	v_max_f32_e32 v76, v77, v76
	v_max_f32_e64 v77, |v9|, |v9|
	v_max_f32_e64 v78, |v8|, |v8|
	v_max_f32_e32 v77, v78, v77
	v_max3_f32 v69, v69, v76, v77
	s_waitcnt vmcnt(3)
	v_mul_f32_e32 v76, v59, v59
	v_mul_f32_e32 v77, v61, v61
	v_fmac_f32_e32 v76, v58, v58
	v_fmac_f32_e32 v77, v60, v60
	v_add_f32_e32 v76, v76, v77
	v_add_f32_e32 v75, v75, v76
	v_max_f32_e64 v76, |v59|, |v59|
	v_max_f32_e64 v77, |v58|, |v58|
	v_max_f32_e32 v76, v77, v76
	v_max_f32_e64 v77, |v61|, |v61|
	v_max_f32_e64 v78, |v60|, |v60|
	v_max_f32_e32 v77, v78, v77
	v_max3_f32 v69, v69, v76, v77
	s_waitcnt vmcnt(2)
	v_mul_f32_e32 v76, v55, v55
	v_mul_f32_e32 v77, v57, v57
	v_fmac_f32_e32 v76, v54, v54
	v_fmac_f32_e32 v77, v56, v56
	v_add_f32_e32 v76, v76, v77
	v_add_f32_e32 v75, v75, v76
	v_max_f32_e64 v76, |v55|, |v55|
	v_max_f32_e64 v77, |v54|, |v54|
	v_max_f32_e32 v76, v77, v76
	v_max_f32_e64 v77, |v57|, |v57|
	v_max_f32_e64 v78, |v56|, |v56|
	v_max_f32_e32 v77, v78, v77
	v_max3_f32 v69, v69, v76, v77
	s_waitcnt vmcnt(1)
	v_mul_f32_e32 v76, v43, v43
	v_mul_f32_e32 v77, v45, v45
	v_fmac_f32_e32 v76, v42, v42
	v_fmac_f32_e32 v77, v44, v44
	v_add_f32_e32 v76, v76, v77
	v_add_f32_e32 v75, v75, v76
	v_max_f32_e64 v76, |v43|, |v43|
	v_max_f32_e64 v77, |v42|, |v42|
	v_max_f32_e32 v76, v77, v76
	v_max_f32_e64 v77, |v45|, |v45|
	v_max_f32_e64 v78, |v44|, |v44|
	v_max_f32_e32 v77, v78, v77
	v_max3_f32 v69, v69, v76, v77
	s_waitcnt vmcnt(0)
	v_mul_f32_e32 v76, v35, v35
	v_mul_f32_e32 v77, v37, v37
	v_fmac_f32_e32 v76, v34, v34
	v_fmac_f32_e32 v77, v36, v36
	v_add_f32_e32 v76, v76, v77
	v_add_f32_e32 v75, v75, v76
	v_max_f32_e64 v76, |v35|, |v35|
	v_max_f32_e64 v77, |v34|, |v34|
	v_max_f32_e32 v76, v77, v76
	v_max_f32_e64 v77, |v37|, |v37|
	v_max_f32_e64 v78, |v36|, |v36|
	v_max_f32_e32 v77, v78, v77
	v_max3_f32 v69, v69, v76, v77
	v_mul_f32_e32 v76, v3, v3
	v_mul_f32_e32 v77, v5, v5
	v_fmac_f32_e32 v76, v2, v2
	v_fmac_f32_e32 v77, v4, v4
	v_add_f32_e32 v76, v76, v77
	v_add_f32_e32 v75, v75, v76
	v_max_f32_e64 v76, |v3|, |v3|
	v_max_f32_e64 v77, |v2|, |v2|
	v_max_f32_e32 v76, v77, v76
	v_max_f32_e64 v77, |v5|, |v5|
	v_max_f32_e64 v80, |v4|, |v4|
	v_max_f32_e32 v77, v80, v77
	v_max3_f32 v69, v69, v76, v77
	s_nop 1
	v_add_f32_dpp v75, v75, v75 quad_perm:[1,0,3,2] row_mask:0xf bank_mask:0xf
	v_max_f32_dpp v69, v69, v69 quad_perm:[1,0,3,2] row_mask:0xf bank_mask:0xf
	s_nop 0
	v_add_f32_dpp v75, v75, v75 quad_perm:[2,3,0,1] row_mask:0xf bank_mask:0xf
	v_max_f32_dpp v69, v69, v69 quad_perm:[2,3,0,1] row_mask:0xf bank_mask:0xf
	s_nop 0
	v_add_f32_dpp v75, v75, v75 row_half_mirror row_mask:0xf bank_mask:0xf
	v_max_f32_dpp v69, v69, v69 row_half_mirror row_mask:0xf bank_mask:0xf
	s_nop 0
	v_add_f32_dpp v75, v75, v75 row_ror:8 row_mask:0xf bank_mask:0xf
	v_max_f32_dpp v69, v69, v69 row_ror:8 row_mask:0xf bank_mask:0xf
	v_cmp_lt_i32_e32 vcc, v156, v154
	s_nop 1
	v_cndmask_b32_e32 v77, v1, v156, vcc
	v_lshlrev_b32_e32 v77, 2, v77
	ds_bpermute_b32 v78, v77, v75
	v_cmp_lt_i32_e32 vcc, v155, v154
	ds_bpermute_b32 v76, v77, v69


	s_waitcnt lgkmcnt(1)
	v_add_f32_e32 v75, v75, v78
	v_cndmask_b32_e32 v77, v1, v155, vcc
	v_lshlrev_b32_e32 v77, 2, v77
	ds_bpermute_b32 v78, v77, v75
	s_waitcnt lgkmcnt(1)
	v_max_f32_e32 v76, v76, v76
	v_max_f32_e32 v69, v69, v76
	ds_bpermute_b32 v76, v77, v69
	s_waitcnt lgkmcnt(1)
	v_add_f32_e32 v75, v75, v78
	v_mul_f32_e32 v75, 0x39800000, v75
	v_mul_f32_e32 v77, 0x4f800000, v75
	v_cmp_gt_f32_e32 vcc, s40, v75
	s_waitcnt lgkmcnt(0)
	v_max_f32_e32 v76, v76, v76
	v_max_f32_e32 v69, v69, v76
	v_cndmask_b32_e32 v75, v75, v77, vcc
	v_sqrt_f32_e32 v77, v75
	v_mul_f32_e32 v69, 0x3e088889, v69
	v_add_u32_e32 v76, -1, v77
	v_fma_f32 v78, -v76, v77, v75
	v_cmp_ge_f32_e64 s[12:13], 0, v78
	v_add_u32_e32 v78, 1, v77
	s_nop 0
	v_cndmask_b32_e64 v76, v77, v76, s[12:13]
	v_fma_f32 v77, -v78, v77, v75
	v_cmp_lt_f32_e64 s[12:13], 0, v77
	s_nop 1
	v_cndmask_b32_e64 v76, v76, v78, s[12:13]
	v_mul_f32_e32 v77, 0x37800000, v76
	v_cndmask_b32_e32 v76, v76, v77, vcc
	v_cmp_class_f32_e32 vcc, v75, v73
	s_nop 1
	v_cndmask_b32_e32 v75, v76, v75, vcc
	v_mul_f32_e32 v75, 0x3eab9f56, v75
	v_min_f32_e32 v69, v75, v69
	v_max_f32_e32 v75, 0xda24260, v69
	v_div_scale_f32 v69, s[12:13], v75, v75, 1.0
	v_rcp_f32_e32 v76, v69
	s_nop 0
	v_fma_f32 v77, -v69, v76, 1.0
	v_fmac_f32_e32 v76, v77, v76
	v_div_scale_f32 v77, vcc, 1.0, v75, 1.0
	v_mul_f32_e32 v78, v77, v76
	v_fma_f32 v79, -v69, v78, v77
	v_fmac_f32_e32 v78, v79, v76
	v_fma_f32 v69, -v69, v78, v77
	v_div_fmas_f32 v69, v69, v76, v78
	v_div_fixup_f32 v69, v69, v75, 1.0
	v_mul_f32_e32 v19, v19, v69
	v_mul_f32_e32 v18, v18, v69
	v_floor_f32_e32 v19, v19
	v_mul_f32_e32 v20, v20, v69
	v_floor_f32_e32 v18, v18
	v_add_f32_e32 v19, 0x41000000, v19
	v_floor_f32_e32 v20, v20
	v_add_f32_e32 v18, 0x41000000, v18
	v_med3_f32 v19, v19, 0, v74
	v_add_f32_e32 v20, 0x41000000, v20
	v_med3_f32 v18, v18, 0, v74
	v_cvt_i32_f32_e32 v19, v19
	v_med3_f32 v20, v20, 0, v74
	v_cvt_i32_f32_e32 v18, v18
	v_cvt_i32_f32_sdwa v20, v20 dst_sel:WORD_1 dst_unused:UNUSED_PAD src0_sel:DWORD
	v_lshlrev_b32_e32 v19, 8, v19
	v_mul_f32_e32 v11, v11, v69
	v_mul_f32_e32 v10, v10, v69
	v_or3_b32 v18, v19, v18, v20
	v_mul_f32_e32 v19, v21, v69
	v_mul_f32_e32 v21, v23, v69
	v_floor_f32_e32 v19, v19
	v_mul_f32_e32 v20, v22, v69
	v_floor_f32_e32 v21, v21
	v_mul_f32_e32 v22, v24, v69
	v_add_f32_e32 v19, 0x41000000, v19
	v_floor_f32_e32 v20, v20
	v_add_f32_e32 v21, 0x41000000, v21
	v_floor_f32_e32 v22, v22
	v_mul_f32_e32 v23, v25, v69
	v_floor_f32_e32 v11, v11
	v_mul_f32_e32 v12, v12, v69
	v_med3_f32 v19, v19, 0, v74
	v_add_f32_e32 v20, 0x41000000, v20
	v_med3_f32 v21, v21, 0, v74
	v_add_f32_e32 v22, 0x41000000, v22
	v_floor_f32_e32 v23, v23
	v_floor_f32_e32 v10, v10
	v_add_f32_e32 v11, 0x41000000, v11
	v_floor_f32_e32 v12, v12
	v_mul_f32_e32 v15, v15, v69
	v_cvt_i32_f32_sdwa v19, v19 dst_sel:BYTE_3 dst_unused:UNUSED_PAD src0_sel:DWORD
	v_med3_f32 v20, v20, 0, v74
	v_cvt_i32_f32_e32 v21, v21
	v_med3_f32 v22, v22, 0, v74
	v_add_f32_e32 v23, 0x41000000, v23
	v_add_f32_e32 v10, 0x41000000, v10
	v_med3_f32 v11, v11, 0, v74
	v_add_f32_e32 v12, 0x41000000, v12
	v_mul_f32_e32 v14, v14, v69
	v_floor_f32_e32 v15, v15
	v_mul_f32_e32 v16, v16, v69
	v_cvt_i32_f32_e32 v20, v20
	v_cvt_i32_f32_sdwa v22, v22 dst_sel:WORD_1 dst_unused:UNUSED_PAD src0_sel:DWORD
	v_med3_f32 v23, v23, 0, v74
	v_med3_f32 v10, v10, 0, v74
	v_cvt_i32_f32_e32 v11, v11
	v_med3_f32 v12, v12, 0, v74
	v_floor_f32_e32 v14, v14
	v_add_f32_e32 v15, 0x41000000, v15
	v_floor_f32_e32 v16, v16
	v_cvt_i32_f32_sdwa v23, v23 dst_sel:BYTE_3 dst_unused:UNUSED_PAD src0_sel:DWORD
	v_cvt_i32_f32_e32 v10, v10
	v_cvt_i32_f32_sdwa v12, v12 dst_sel:WORD_1 dst_unused:UNUSED_PAD src0_sel:DWORD
	v_add_f32_e32 v14, 0x41000000, v14
	v_med3_f32 v15, v15, 0, v74
	v_add_f32_e32 v16, 0x41000000, v16
	v_med3_f32 v14, v14, 0, v74
	v_cvt_i32_f32_e32 v15, v15
	v_med3_f32 v16, v16, 0, v74
	v_bitop3_b32 v18, v18, s41, v19 bitop3:0x36
	v_lshlrev_b32_e32 v19, 8, v21
	v_cvt_i32_f32_e32 v14, v14
	v_cvt_i32_f32_sdwa v16, v16 dst_sel:WORD_1 dst_unused:UNUSED_PAD src0_sel:DWORD
	v_or3_b32 v19, v19, v20, v22
	v_lshlrev_b32_e32 v11, 8, v11
	v_or_b32_e32 v20, v19, v23
	v_bitop3_b32 v19, v19, s41, v23 bitop3:0x36
	v_or3_b32 v10, v11, v10, v12
	v_mul_f32_e32 v11, v13, v69
	v_mul_f32_e32 v13, v63, v69
	v_cndmask_b32_e64 v19, v19, v20, s[10:11]
	v_floor_f32_e32 v11, v11
	v_mul_f32_e32 v12, v62, v69
	v_floor_f32_e32 v13, v13
	v_mul_f32_e32 v20, v64, v69
	v_lshlrev_b32_e32 v15, 8, v15
	v_add_f32_e32 v11, 0x41000000, v11
	v_floor_f32_e32 v12, v12
	v_add_f32_e32 v13, 0x41000000, v13
	v_floor_f32_e32 v20, v20
	v_or3_b32 v14, v15, v14, v16
	v_mul_f32_e32 v15, v17, v69
	v_mul_f32_e32 v7, v7, v69
	v_med3_f32 v11, v11, 0, v74
	v_add_f32_e32 v12, 0x41000000, v12
	v_med3_f32 v13, v13, 0, v74
	v_add_f32_e32 v20, 0x41000000, v20
	v_floor_f32_e32 v15, v15
	v_mul_f32_e32 v6, v6, v69
	v_floor_f32_e32 v7, v7
	v_mul_f32_e32 v8, v8, v69
	v_cvt_i32_f32_sdwa v11, v11 dst_sel:BYTE_3 dst_unused:UNUSED_PAD src0_sel:DWORD
	v_med3_f32 v12, v12, 0, v74
	v_cvt_i32_f32_e32 v13, v13
	v_med3_f32 v20, v20, 0, v74
	v_add_f32_e32 v15, 0x41000000, v15
	v_floor_f32_e32 v6, v6
	v_add_f32_e32 v7, 0x41000000, v7
	v_floor_f32_e32 v8, v8
	v_cvt_i32_f32_e32 v12, v12
	v_cvt_i32_f32_sdwa v20, v20 dst_sel:WORD_1 dst_unused:UNUSED_PAD src0_sel:DWORD
	v_med3_f32 v15, v15, 0, v74
	v_add_f32_e32 v6, 0x41000000, v6
	v_med3_f32 v7, v7, 0, v74
	v_add_f32_e32 v8, 0x41000000, v8
	v_cvt_i32_f32_sdwa v15, v15 dst_sel:BYTE_3 dst_unused:UNUSED_PAD src0_sel:DWORD
	v_med3_f32 v6, v6, 0, v74
	v_cvt_i32_f32_e32 v7, v7
	v_med3_f32 v8, v8, 0, v74
	v_cvt_i32_f32_e32 v6, v6
	v_cvt_i32_f32_sdwa v8, v8 dst_sel:WORD_1 dst_unused:UNUSED_PAD src0_sel:DWORD
	v_mul_f32_e32 v21, v65, v69
	v_bitop3_b32 v10, v10, s41, v11 bitop3:0x36
	v_lshlrev_b32_e32 v11, 8, v13
	v_floor_f32_e32 v21, v21
	v_or3_b32 v11, v11, v12, v20
	v_mul_f32_e32 v20, v51, v69
	v_mul_f32_e32 v9, v9, v69
	v_add_f32_e32 v21, 0x41000000, v21
	v_mul_f32_e32 v13, v50, v69
	v_floor_f32_e32 v20, v20
	v_mul_f32_e32 v22, v52, v69
	v_floor_f32_e32 v9, v9
	v_bitop3_b32 v14, v14, s41, v15 bitop3:0x36
	v_lshlrev_b32_e32 v7, 8, v7
	v_mul_f32_e32 v15, v59, v69
	v_med3_f32 v21, v21, 0, v74
	v_floor_f32_e32 v13, v13
	v_add_f32_e32 v20, 0x41000000, v20
	v_floor_f32_e32 v22, v22
	v_add_f32_e32 v9, 0x41000000, v9
	v_or3_b32 v6, v7, v6, v8
	v_mul_f32_e32 v8, v58, v69
	v_floor_f32_e32 v15, v15
	v_mul_f32_e32 v16, v60, v69
	v_cvt_i32_f32_sdwa v21, v21 dst_sel:BYTE_3 dst_unused:UNUSED_PAD src0_sel:DWORD
	v_add_f32_e32 v13, 0x41000000, v13
	v_med3_f32 v20, v20, 0, v74
	v_add_f32_e32 v22, 0x41000000, v22
	v_med3_f32 v9, v9, 0, v74
	v_floor_f32_e32 v8, v8
	v_add_f32_e32 v15, 0x41000000, v15
	v_floor_f32_e32 v16, v16
	v_med3_f32 v13, v13, 0, v74
	v_cvt_i32_f32_e32 v20, v20
	v_med3_f32 v22, v22, 0, v74
	v_cvt_i32_f32_sdwa v9, v9 dst_sel:BYTE_3 dst_unused:UNUSED_PAD src0_sel:DWORD
	v_add_f32_e32 v8, 0x41000000, v8
	v_med3_f32 v15, v15, 0, v74
	v_add_f32_e32 v16, 0x41000000, v16
	v_cvt_i32_f32_e32 v13, v13
	v_cvt_i32_f32_sdwa v22, v22 dst_sel:WORD_1 dst_unused:UNUSED_PAD src0_sel:DWORD
	v_med3_f32 v8, v8, 0, v74
	v_cvt_i32_f32_e32 v15, v15
	v_med3_f32 v16, v16, 0, v74
	v_cvt_i32_f32_e32 v8, v8
	v_cvt_i32_f32_sdwa v16, v16 dst_sel:WORD_1 dst_unused:UNUSED_PAD src0_sel:DWORD
	v_or_b32_e32 v12, v11, v21
	v_bitop3_b32 v11, v11, s41, v21 bitop3:0x36
	v_cndmask_b32_e64 v11, v11, v12, s[10:11]
	v_lshlrev_b32_e32 v12, 8, v20
	v_or_b32_e32 v7, v6, v9
	v_bitop3_b32 v6, v6, s41, v9 bitop3:0x36
	v_or3_b32 v12, v12, v13, v22
	v_mul_f32_e32 v13, v53, v69
	v_mul_f32_e32 v21, v39, v69
	v_cndmask_b32_e64 v6, v6, v7, s[10:11]
	v_lshlrev_b32_e32 v7, 8, v15
	v_floor_f32_e32 v13, v13
	v_mul_f32_e32 v20, v38, v69
	v_floor_f32_e32 v21, v21
	v_mul_f32_e32 v22, v40, v69
	v_or3_b32 v7, v7, v8, v16
	v_mul_f32_e32 v8, v61, v69
	v_mul_f32_e32 v15, v55, v69
	v_add_f32_e32 v13, 0x41000000, v13
	v_floor_f32_e32 v20, v20
	v_add_f32_e32 v21, 0x41000000, v21
	v_floor_f32_e32 v22, v22
	v_mul_f32_e32 v23, v41, v69
	v_floor_f32_e32 v8, v8
	v_mul_f32_e32 v9, v54, v69
	v_floor_f32_e32 v15, v15
	v_mul_f32_e32 v16, v56, v69
	v_med3_f32 v13, v13, 0, v74
	v_add_f32_e32 v20, 0x41000000, v20
	v_med3_f32 v21, v21, 0, v74
	v_add_f32_e32 v22, 0x41000000, v22
	v_floor_f32_e32 v23, v23
	v_add_f32_e32 v8, 0x41000000, v8
	v_floor_f32_e32 v9, v9
	v_add_f32_e32 v15, 0x41000000, v15
	v_floor_f32_e32 v16, v16
	v_cvt_i32_f32_sdwa v13, v13 dst_sel:BYTE_3 dst_unused:UNUSED_PAD src0_sel:DWORD
	v_med3_f32 v20, v20, 0, v74
	v_cvt_i32_f32_e32 v21, v21
	v_med3_f32 v22, v22, 0, v74
	v_add_f32_e32 v23, 0x41000000, v23
	v_med3_f32 v8, v8, 0, v74
	v_add_f32_e32 v9, 0x41000000, v9
	v_med3_f32 v15, v15, 0, v74
	v_add_f32_e32 v16, 0x41000000, v16
	v_cvt_i32_f32_e32 v20, v20
	v_cvt_i32_f32_sdwa v22, v22 dst_sel:WORD_1 dst_unused:UNUSED_PAD src0_sel:DWORD
	v_med3_f32 v23, v23, 0, v74
	v_cvt_i32_f32_sdwa v8, v8 dst_sel:BYTE_3 dst_unused:UNUSED_PAD src0_sel:DWORD
	v_med3_f32 v9, v9, 0, v74
	v_cvt_i32_f32_e32 v15, v15
	v_med3_f32 v16, v16, 0, v74
	v_cvt_i32_f32_sdwa v23, v23 dst_sel:BYTE_3 dst_unused:UNUSED_PAD src0_sel:DWORD
	v_cvt_i32_f32_e32 v9, v9
	v_cvt_i32_f32_sdwa v16, v16 dst_sel:WORD_1 dst_unused:UNUSED_PAD src0_sel:DWORD
	v_bitop3_b32 v12, v12, s41, v13 bitop3:0x36
	v_lshlrev_b32_e32 v13, 8, v21
	v_or3_b32 v13, v13, v20, v22
	v_mul_f32_e32 v17, v57, v69
	v_bitop3_b32 v7, v7, s41, v8 bitop3:0x36
	v_lshlrev_b32_e32 v8, 8, v15
	v_or_b32_e32 v20, v13, v23
	v_bitop3_b32 v13, v13, s41, v23 bitop3:0x36
	v_floor_f32_e32 v17, v17
	v_or3_b32 v8, v8, v9, v16
	v_mul_f32_e32 v16, v43, v69
	v_cndmask_b32_e64 v13, v13, v20, s[10:11]
	v_add_f32_e32 v17, 0x41000000, v17
	v_mul_f32_e32 v15, v42, v69
	v_floor_f32_e32 v16, v16
	v_mul_f32_e32 v20, v44, v69
	v_med3_f32 v17, v17, 0, v74
	v_floor_f32_e32 v15, v15
	v_add_f32_e32 v16, 0x41000000, v16
	v_floor_f32_e32 v20, v20
	v_cvt_i32_f32_sdwa v17, v17 dst_sel:BYTE_3 dst_unused:UNUSED_PAD src0_sel:DWORD
	v_add_f32_e32 v15, 0x41000000, v15
	v_med3_f32 v16, v16, 0, v74
	v_add_f32_e32 v20, 0x41000000, v20
	v_med3_f32 v15, v15, 0, v74
	v_cvt_i32_f32_e32 v16, v16
	v_med3_f32 v20, v20, 0, v74
	v_cvt_i32_f32_e32 v15, v15
	v_cvt_i32_f32_sdwa v20, v20 dst_sel:WORD_1 dst_unused:UNUSED_PAD src0_sel:DWORD
	v_mul_f32_e32 v31, v31, v69
	v_mul_f32_e32 v30, v30, v69
	v_floor_f32_e32 v31, v31
	v_mul_f32_e32 v32, v32, v69
	v_or_b32_e32 v9, v8, v17
	v_bitop3_b32 v8, v8, s41, v17 bitop3:0x36
	v_floor_f32_e32 v30, v30
	v_add_f32_e32 v31, 0x41000000, v31
	v_floor_f32_e32 v32, v32
	v_cndmask_b32_e64 v8, v8, v9, s[10:11]
	v_lshlrev_b32_e32 v9, 8, v16
	v_add_f32_e32 v30, 0x41000000, v30
	v_med3_f32 v31, v31, 0, v74
	v_add_f32_e32 v32, 0x41000000, v32
	v_or3_b32 v9, v9, v15, v20
	v_mul_f32_e32 v15, v45, v69
	v_mul_f32_e32 v17, v35, v69
	v_med3_f32 v30, v30, 0, v74
	v_cvt_i32_f32_e32 v31, v31
	v_med3_f32 v32, v32, 0, v74
	v_floor_f32_e32 v15, v15
	v_mul_f32_e32 v16, v34, v69
	v_floor_f32_e32 v17, v17
	v_mul_f32_e32 v20, v36, v69
	v_mul_f32_e32 v3, v3, v69
	v_cvt_i32_f32_e32 v30, v30
	v_cvt_i32_f32_sdwa v32, v32 dst_sel:WORD_1 dst_unused:UNUSED_PAD src0_sel:DWORD
	v_add_f32_e32 v15, 0x41000000, v15
	v_floor_f32_e32 v16, v16
	v_add_f32_e32 v17, 0x41000000, v17
	v_floor_f32_e32 v20, v20
	v_mul_f32_e32 v21, v37, v69
	v_mul_f32_e32 v2, v2, v69
	v_floor_f32_e32 v3, v3
	v_mul_f32_e32 v4, v4, v69
	v_mul_f32_e32 v47, v47, v69
	v_med3_f32 v15, v15, 0, v74
	v_add_f32_e32 v16, 0x41000000, v16
	v_med3_f32 v17, v17, 0, v74
	v_add_f32_e32 v20, 0x41000000, v20
	v_floor_f32_e32 v21, v21
	v_floor_f32_e32 v2, v2
	v_add_f32_e32 v3, 0x41000000, v3
	v_floor_f32_e32 v4, v4
	v_mul_f32_e32 v5, v5, v69
	v_mul_f32_e32 v46, v46, v69
	v_floor_f32_e32 v47, v47
	v_mul_f32_e32 v48, v48, v69
	v_cvt_i32_f32_sdwa v15, v15 dst_sel:BYTE_3 dst_unused:UNUSED_PAD src0_sel:DWORD
	v_med3_f32 v16, v16, 0, v74
	v_cvt_i32_f32_e32 v17, v17
	v_med3_f32 v20, v20, 0, v74
	v_add_f32_e32 v21, 0x41000000, v21
	v_add_f32_e32 v2, 0x41000000, v2
	v_med3_f32 v3, v3, 0, v74
	v_add_f32_e32 v4, 0x41000000, v4
	v_floor_f32_e32 v5, v5
	v_floor_f32_e32 v46, v46
	v_add_f32_e32 v47, 0x41000000, v47
	v_floor_f32_e32 v48, v48
	v_mul_f32_e32 v49, v49, v69
	v_lshlrev_b32_e32 v31, 8, v31
	v_mul_f32_e32 v27, v27, v69
	v_cvt_i32_f32_e32 v16, v16
	v_cvt_i32_f32_sdwa v20, v20 dst_sel:WORD_1 dst_unused:UNUSED_PAD src0_sel:DWORD
	v_med3_f32 v21, v21, 0, v74
	v_med3_f32 v2, v2, 0, v74
	v_cvt_i32_f32_e32 v3, v3
	v_med3_f32 v4, v4, 0, v74
	v_add_f32_e32 v5, 0x41000000, v5
	v_add_f32_e32 v46, 0x41000000, v46
	v_med3_f32 v47, v47, 0, v74
	v_add_f32_e32 v48, 0x41000000, v48
	v_floor_f32_e32 v49, v49
	v_or3_b32 v30, v31, v30, v32
	v_mul_f32_e32 v31, v33, v69
	v_mul_f32_e32 v26, v26, v69
	v_floor_f32_e32 v27, v27
	v_mul_f32_e32 v28, v28, v69
	v_cvt_i32_f32_sdwa v21, v21 dst_sel:BYTE_3 dst_unused:UNUSED_PAD src0_sel:DWORD
	v_cvt_i32_f32_e32 v2, v2
	v_cvt_i32_f32_sdwa v4, v4 dst_sel:WORD_1 dst_unused:UNUSED_PAD src0_sel:DWORD
	v_med3_f32 v5, v5, 0, v74
	v_med3_f32 v46, v46, 0, v74
	v_cvt_i32_f32_e32 v47, v47
	v_med3_f32 v48, v48, 0, v74
	v_add_f32_e32 v49, 0x41000000, v49
	v_floor_f32_e32 v31, v31
	v_floor_f32_e32 v26, v26
	v_add_f32_e32 v27, 0x41000000, v27
	v_floor_f32_e32 v28, v28
	v_mul_f32_e32 v29, v29, v69
	v_cvt_i32_f32_sdwa v5, v5 dst_sel:BYTE_3 dst_unused:UNUSED_PAD src0_sel:DWORD
	v_cvt_i32_f32_e32 v46, v46
	v_cvt_i32_f32_sdwa v48, v48 dst_sel:WORD_1 dst_unused:UNUSED_PAD src0_sel:DWORD
	v_med3_f32 v49, v49, 0, v74
	v_add_f32_e32 v31, 0x41000000, v31
	v_add_f32_e32 v26, 0x41000000, v26
	v_med3_f32 v27, v27, 0, v74
	v_add_f32_e32 v28, 0x41000000, v28
	v_floor_f32_e32 v29, v29
	v_bitop3_b32 v9, v9, s41, v15 bitop3:0x36
	v_lshlrev_b32_e32 v15, 8, v17
	v_cvt_i32_f32_sdwa v49, v49 dst_sel:BYTE_3 dst_unused:UNUSED_PAD src0_sel:DWORD
	v_med3_f32 v31, v31, 0, v74
	v_med3_f32 v26, v26, 0, v74
	v_cvt_i32_f32_e32 v27, v27
	v_med3_f32 v28, v28, 0, v74
	v_add_f32_e32 v29, 0x41000000, v29
	v_or3_b32 v15, v15, v16, v20
	v_lshlrev_b32_e32 v3, 8, v3
	v_cvt_i32_f32_sdwa v31, v31 dst_sel:BYTE_3 dst_unused:UNUSED_PAD src0_sel:DWORD
	v_cvt_i32_f32_e32 v26, v26
	v_cvt_i32_f32_sdwa v28, v28 dst_sel:WORD_1 dst_unused:UNUSED_PAD src0_sel:DWORD
	v_med3_f32 v29, v29, 0, v74
	v_or_b32_e32 v16, v15, v21
	v_bitop3_b32 v15, v15, s41, v21 bitop3:0x36
	v_or3_b32 v2, v3, v2, v4
	v_lshlrev_b32_e32 v47, 8, v47
	v_cvt_i32_f32_sdwa v29, v29 dst_sel:BYTE_3 dst_unused:UNUSED_PAD src0_sel:DWORD
	v_cndmask_b32_e64 v15, v15, v16, s[10:11]
	v_bitop3_b32 v16, v2, s41, v5 bitop3:0x36
	v_mov_b32_e32 v2, s14
	v_mov_b32_e32 v3, s31
	v_or3_b32 v46, v47, v46, v48
	v_cndmask_b32_e64 v3, v2, v3, s[10:11]
	v_mov_b32_e32 v2, s3
	v_mov_b32_e32 v4, s30
	v_or_b32_e32 v47, v46, v49
	v_bitop3_b32 v46, v46, s41, v49 bitop3:0x36
	v_lshlrev_b32_e32 v27, 8, v27
	v_cndmask_b32_e64 v2, v2, v4, s[10:11]
	v_lshlrev_b64 v[4:5], 8, v[70:71]
	v_cndmask_b32_e64 v46, v46, v47, s[10:11]
	v_bitop3_b32 v30, v30, s41, v31 bitop3:0x36
	v_or3_b32 v26, v27, v26, v28
	v_lshl_add_u64 v[2:3], v[2:3], 0, v[4:5]
	v_mov_b32_e32 v69, v67
	v_or_b32_e32 v27, v26, v29
	v_bitop3_b32 v26, v26, s41, v29 bitop3:0x36
	v_lshl_add_u64 v[2:3], v[2:3], 0, v[68:69]
	v_lshl_or_b32 v4, v30, 4, v46
	v_cndmask_b32_e64 v26, v26, v27, s[10:11]
	global_store_dword v[2:3], v4, off
	v_add_co_u32_e32 v4, vcc, s42, v2
	v_lshl_or_b32 v17, v18, 4, v26
	s_nop 0
	v_addc_co_u32_e32 v5, vcc, 0, v3, vcc
	global_store_dword v[4:5], v17, off
	v_add_co_u32_e32 v4, vcc, s43, v2
	v_lshl_or_b32 v10, v10, 4, v19
	s_nop 0
	v_addc_co_u32_e32 v5, vcc, 0, v3, vcc
	global_store_dword v[4:5], v10, off
	v_add_co_u32_e32 v4, vcc, s52, v2
	v_lshl_or_b32 v10, v12, 4, v11
	s_nop 0
	v_addc_co_u32_e32 v5, vcc, 0, v3, vcc
	global_store_dword v[4:5], v10, off
	v_add_co_u32_e32 v4, vcc, s53, v2
	v_lshl_or_b32 v10, v14, 4, v13
	s_nop 0
	v_addc_co_u32_e32 v5, vcc, 0, v3, vcc
	global_store_dword v[4:5], v10, off
	v_add_co_u32_e32 v4, vcc, 0x1400000, v2
	v_lshl_or_b32 v6, v7, 4, v6
	s_nop 0
	v_addc_co_u32_e32 v5, vcc, 0, v3, vcc
	global_store_dword v[4:5], v6, off
	v_add_co_u32_e32 v4, vcc, 0x1800000, v2
	v_lshl_or_b32 v6, v9, 4, v8
	s_nop 0
	v_addc_co_u32_e32 v5, vcc, 0, v3, vcc
	v_add_co_u32_e32 v2, vcc, 0x1c00000, v2
	global_store_dword v[4:5], v6, off
	v_lshl_or_b32 v4, v16, 4, v15
	v_addc_co_u32_e32 v3, vcc, 0, v3, vcc
	global_store_dword v[2:3], v4, off
	s_and_saveexec_b64 s[12:13], s[8:9]
	s_cbranch_execz .LBB0_1387
	v_mov_b32_e32 v2, s29
	v_mov_b32_e32 v3, s35
	v_cndmask_b32_e64 v3, v2, v3, s[10:11]
	v_mov_b32_e32 v2, s28
	v_mov_b32_e32 v4, s34
	v_cndmask_b32_e64 v2, v2, v4, s[10:11]
	v_lshl_add_u64 v[2:3], v[70:71], 2, v[2:3]
	global_store_dword v[2:3], v75, off
	s_branch .LBB0_1387

.LBB0_1809:
	s_lshl_b32 s56, s47, 5
	v_add_u32_e32 v2, s56, v72
	v_ashrrev_i32_e32 v3, 31, v2
	v_lshlrev_b64 v[2:3], 12, v[2:3]
	v_lshl_add_u64 v[10:11], v[38:39], 0, v[2:3]
	s_waitcnt lgkmcnt(0)
	s_barrier
	global_load_dwordx4 v[2:5], v[10:11], off
	global_load_dwordx4 v[6:9], v[10:11], off offset:16
	s_waitcnt vmcnt(2) lgkmcnt(0)
	s_mov_b32 s60, s96
	s_mov_b32 s61, s97
	s_mov_b64 s[66:67], s[98:99]
	s_mov_b64 s[68:69], s[96:97]
	s_mov_b64 s[70:71], s[98:99]
	s_movk_i32 s72, 0x1000
	s_movk_i32 s73, 0x3fff
	s_movk_i32 s74, 0x2000
	s_movk_i32 s75, 0x3000
	s_mov_b32 s76, 0xf800000
	s_mov_b32 s77, 0x8080808
	s_mov_b32 s78, 0x400000
	s_mov_b32 s79, 0x800000
	s_mov_b32 s80, 0xc00000
	s_mov_b32 s81, 0x1000000
	v_cmp_eq_u32_e64 s[82:83], 0, v1
	s_mov_b64 s[86:87], exec
	v_mul_f32_e32 v202, v207, v207
	v_mul_f32_e32 v203, v209, v209
	v_max_f32_e64 v204, |v207|, |v207|
	v_max_f32_e64 v205, |v206|, |v206|
	v_max_f32_e64 v214, |v209|, |v209|
	v_max_f32_e64 v215, |v208|, |v208|
	s_nop 0
	v_mul_f32_e32 v216, v191, v191
	v_mul_f32_e32 v217, v193, v193
	s_nop 0
	v_mul_f32_e32 v229, v187, v187
	v_mul_f32_e32 v235, v189, v189
	v_fmac_f32_e32 v202, v206, v206
	v_fmac_f32_e32 v203, v208, v208
	v_max_f32_e32 v204, v205, v204
	v_max_f32_e32 v205, v215, v214
	v_fmac_f32_e32 v216, v190, v190
	v_fmac_f32_e32 v217, v192, v192
	v_max_f32_e64 v218, |v191|, |v191|
	v_max_f32_e64 v219, |v190|, |v190|
	v_max_f32_e64 v236, |v187|, |v187|
	v_max_f32_e64 v237, |v186|, |v186|
	s_nop 0
	v_mul_f32_e32 v240, v179, v179
	v_mul_f32_e32 v241, v181, v181
	v_fmac_f32_e32 v229, v186, v186
	v_fmac_f32_e32 v235, v188, v188
	v_add_f32_e32 v202, v202, v203
	v_max3_f32 v203, v204, 0, v205
	v_add_f32_e32 v204, v216, v217
	v_max_f32_e32 v214, v219, v218
	v_max_f32_e32 v218, v237, v236
	v_fmac_f32_e32 v240, v178, v178
	v_fmac_f32_e32 v241, v180, v180
	s_nop 0
	v_mul_f32_e32 v236, v183, v183
	v_mul_f32_e32 v237, v185, v185
	v_add_f32_e32 v205, v229, v235
	v_add_f32_e32 v202, v202, v204
	v_max_f32_e64 v220, |v193|, |v193|
	v_max_f32_e64 v221, |v192|, |v192|
	v_add_f32_e32 v216, v240, v241
	v_fmac_f32_e32 v236, v182, v182
	v_fmac_f32_e32 v237, v184, v184
	v_add_f32_e32 v202, v202, v205
	v_max_f32_e64 v238, |v189|, |v189|
	v_max_f32_e64 v239, |v188|, |v188|
	v_max_f32_e32 v215, v221, v220
	v_add_f32_e32 v202, v202, v216
	v_add_f32_e32 v204, v236, v237
	v_max_f32_e64 v242, |v179|, |v179|
	v_max_f32_e64 v243, |v178|, |v178|
	v_max_f32_e64 v244, |v181|, |v181|
	v_max_f32_e64 v245, |v180|, |v180|
	v_max_f32_e32 v219, v239, v238
	v_max3_f32 v203, v203, v214, v215
	v_add_f32_e32 v202, v202, v204
	v_max_f32_e64 v204, |v183|, |v183|
	v_max_f32_e64 v205, |v182|, |v182|
	v_max_f32_e32 v220, v243, v242
	v_max_f32_e32 v221, v245, v244
	v_max3_f32 v203, v203, v218, v219
	v_max_f32_e32 v204, v205, v204
	v_max_f32_e64 v205, |v185|, |v185|
	v_max_f32_e64 v214, |v184|, |v184|
	v_max3_f32 v203, v203, v220, v221
	v_max_f32_e32 v205, v214, v205
	v_max3_f32 v203, v203, v204, v205
	v_mov_b32_e32 v218, v86
	v_mov_b32_e32 v219, v87
	v_mov_b32_e32 v220, v88
	v_mov_b32_e32 v221, v89
	v_mov_b32_e32 v214, v90
	v_mov_b32_e32 v215, v91
	v_mov_b32_e32 v216, v92
	v_mov_b32_e32 v217, v93
	v_cmp_lt_i32_e32 vcc, v157, v154
	s_nop 0
	v_mul_f32_e32 v204, v171, v171
	v_mul_f32_e32 v194, v173, v173
	v_fmac_f32_e32 v204, v170, v170
	v_fmac_f32_e32 v194, v172, v172
	v_add_f32_e32 v194, v204, v194
	v_add_f32_e32 v194, v202, v194
	v_max_f32_e64 v195, |v171|, |v171|
	v_max_f32_e64 v202, |v170|, |v170|
	v_max_f32_e32 v195, v202, v195
	v_max_f32_e64 v202, |v173|, |v173|
	v_max_f32_e64 v204, |v172|, |v172|
	v_max_f32_e32 v202, v204, v202
	v_max3_f32 v195, v203, v195, v202
	s_nop 0
	v_mul_f32_e32 v202, v223, v223
	v_mul_f32_e32 v203, v225, v225
	v_fmac_f32_e32 v202, v222, v222
	v_fmac_f32_e32 v203, v224, v224
	v_add_f32_e32 v202, v202, v203
	v_add_f32_e32 v194, v194, v202
	v_max_f32_e64 v202, |v223|, |v223|
	v_max_f32_e64 v203, |v222|, |v222|
	v_max_f32_e32 v202, v203, v202
	v_max_f32_e64 v203, |v225|, |v225|
	v_max_f32_e64 v204, |v224|, |v224|
	v_max_f32_e32 v203, v204, v203
	v_max3_f32 v229, v195, v202, v203
	v_mov_b32_e32 v202, v94
	v_mov_b32_e32 v203, v95
	v_mov_b32_e32 v204, v96
	v_mov_b32_e32 v205, v97
	s_nop 0
	v_mul_f32_e32 v195, v211, v211
	v_mul_f32_e32 v235, v213, v213
	v_fmac_f32_e32 v195, v210, v210
	v_fmac_f32_e32 v235, v212, v212
	v_add_f32_e32 v195, v195, v235
	v_add_f32_e32 v235, v194, v195
	v_max_f32_e64 v194, |v211|, |v211|
	v_max_f32_e64 v195, |v210|, |v210|
	v_max_f32_e32 v236, v195, v194
	v_max_f32_e64 v194, |v213|, |v213|
	v_max_f32_e64 v195, |v212|, |v212|
	v_max_f32_e32 v237, v195, v194
	v_mov_b32_e32 v194, v98
	v_mov_b32_e32 v195, v99
	v_mov_b32_e32 v196, v100
	v_mov_b32_e32 v197, v101
	v_max3_f32 v229, v229, v236, v237
	s_nop 0
	v_mul_f32_e32 v236, v199, v199
	v_mul_f32_e32 v237, v201, v201
	v_fmac_f32_e32 v236, v198, v198
	v_fmac_f32_e32 v237, v200, v200
	v_add_f32_e32 v236, v236, v237
	v_add_f32_e32 v235, v235, v236
	v_max_f32_e64 v236, |v199|, |v199|
	v_max_f32_e64 v237, |v198|, |v198|
	v_max_f32_e32 v236, v237, v236
	v_max_f32_e64 v237, |v201|, |v201|
	v_max_f32_e64 v238, |v200|, |v200|
	v_max_f32_e32 v237, v238, v237
	v_max3_f32 v229, v229, v236, v237
	s_nop 0
	v_mul_f32_e32 v236, v175, v175
	v_mul_f32_e32 v237, v177, v177
	v_fmac_f32_e32 v236, v174, v174
	v_fmac_f32_e32 v237, v176, v176
	v_add_f32_e32 v236, v236, v237
	v_add_f32_e32 v235, v235, v236
	v_max_f32_e64 v236, |v175|, |v175|
	v_max_f32_e64 v237, |v174|, |v174|
	v_max_f32_e32 v236, v237, v236
	v_max_f32_e64 v237, |v177|, |v177|
	v_max_f32_e64 v238, |v176|, |v176|
	v_max_f32_e32 v237, v238, v237
	v_max3_f32 v229, v229, v236, v237
	s_nop 0
	v_mul_f32_e32 v236, v167, v167
	v_mul_f32_e32 v237, v169, v169
	v_fmac_f32_e32 v236, v166, v166
	v_fmac_f32_e32 v237, v168, v168
	v_add_f32_e32 v236, v236, v237
	v_add_f32_e32 v235, v235, v236
	v_max_f32_e64 v236, |v167|, |v167|
	v_max_f32_e64 v237, |v166|, |v166|
	v_max_f32_e32 v236, v237, v236
	v_max_f32_e64 v237, |v169|, |v169|
	v_max_f32_e64 v238, |v168|, |v168|
	v_max_f32_e32 v237, v238, v237
	v_max3_f32 v229, v229, v236, v237
	s_nop 0
	v_mul_f32_e32 v236, v219, v219
	v_mul_f32_e32 v237, v221, v221
	v_fmac_f32_e32 v236, v218, v218
	v_fmac_f32_e32 v237, v220, v220
	v_add_f32_e32 v236, v236, v237
	v_add_f32_e32 v235, v235, v236
	v_max_f32_e64 v236, |v219|, |v219|
	v_max_f32_e64 v237, |v218|, |v218|
	v_max_f32_e32 v236, v237, v236
	v_max_f32_e64 v237, |v221|, |v221|
	v_max_f32_e64 v238, |v220|, |v220|
	v_max_f32_e32 v237, v238, v237
	v_max3_f32 v229, v229, v236, v237
	s_nop 0
	v_mul_f32_e32 v236, v215, v215
	v_mul_f32_e32 v237, v217, v217
	v_fmac_f32_e32 v236, v214, v214
	v_fmac_f32_e32 v237, v216, v216
	v_add_f32_e32 v236, v236, v237
	v_add_f32_e32 v235, v235, v236
	v_max_f32_e64 v236, |v215|, |v215|
	v_max_f32_e64 v237, |v214|, |v214|
	v_max_f32_e32 v236, v237, v236
	v_max_f32_e64 v237, |v217|, |v217|
	v_max_f32_e64 v238, |v216|, |v216|
	v_max_f32_e32 v237, v238, v237
	v_max3_f32 v229, v229, v236, v237
	s_nop 0
	v_mul_f32_e32 v236, v203, v203
	v_mul_f32_e32 v237, v205, v205
	v_fmac_f32_e32 v236, v202, v202
	v_fmac_f32_e32 v237, v204, v204
	v_add_f32_e32 v236, v236, v237
	v_add_f32_e32 v235, v235, v236
	v_max_f32_e64 v236, |v203|, |v203|
	v_max_f32_e64 v237, |v202|, |v202|
	v_max_f32_e32 v236, v237, v236
	v_max_f32_e64 v237, |v205|, |v205|
	v_max_f32_e64 v238, |v204|, |v204|
	v_max_f32_e32 v237, v238, v237
	v_max3_f32 v229, v229, v236, v237
	s_nop 0
	v_mul_f32_e32 v236, v195, v195
	v_mul_f32_e32 v237, v197, v197
	v_fmac_f32_e32 v236, v194, v194
	v_fmac_f32_e32 v237, v196, v196
	v_add_f32_e32 v236, v236, v237
	v_add_f32_e32 v235, v235, v236
	v_max_f32_e64 v236, |v195|, |v195|
	v_max_f32_e64 v237, |v194|, |v194|
	v_max_f32_e32 v236, v237, v236
	v_max_f32_e64 v237, |v197|, |v197|
	v_max_f32_e64 v238, |v196|, |v196|
	v_max_f32_e32 v237, v238, v237
	v_max3_f32 v229, v229, v236, v237
	v_mul_f32_e32 v236, v163, v163
	v_mul_f32_e32 v237, v165, v165
	v_fmac_f32_e32 v236, v162, v162
	v_fmac_f32_e32 v237, v164, v164
	v_add_f32_e32 v236, v236, v237
	v_add_f32_e32 v235, v235, v236
	v_max_f32_e64 v236, |v163|, |v163|
	v_max_f32_e64 v237, |v162|, |v162|
	v_max_f32_e32 v236, v237, v236
	v_max_f32_e64 v237, |v165|, |v165|
	v_max_f32_e64 v240, |v164|, |v164|
	v_max_f32_e32 v237, v240, v237
	v_max3_f32 v229, v229, v236, v237
	s_nop 1
	v_add_f32_dpp v235, v235, v235 quad_perm:[1,0,3,2] row_mask:0xf bank_mask:0xf
	v_max_f32_dpp v229, v229, v229 quad_perm:[1,0,3,2] row_mask:0xf bank_mask:0xf
	s_nop 0
	v_add_f32_dpp v235, v235, v235 quad_perm:[2,3,0,1] row_mask:0xf bank_mask:0xf
	v_max_f32_dpp v229, v229, v229 quad_perm:[2,3,0,1] row_mask:0xf bank_mask:0xf
	s_nop 0
	v_add_f32_dpp v235, v235, v235 row_half_mirror row_mask:0xf bank_mask:0xf
	v_max_f32_dpp v229, v229, v229 row_half_mirror row_mask:0xf bank_mask:0xf
	s_nop 0
	v_add_f32_dpp v235, v235, v235 row_ror:8 row_mask:0xf bank_mask:0xf
	v_max_f32_dpp v229, v229, v229 row_ror:8 row_mask:0xf bank_mask:0xf
	v_cmp_lt_i32_e32 vcc, v156, v154
	s_nop 1
	v_cndmask_b32_e32 v237, v1, v156, vcc
	v_lshlrev_b32_e32 v237, 2, v237
	ds_bpermute_b32 v238, v237, v235
	v_cmp_lt_i32_e32 vcc, v155, v154
	ds_bpermute_b32 v236, v237, v229
	s_waitcnt lgkmcnt(1)
	v_add_f32_e32 v235, v235, v238
	v_cndmask_b32_e32 v237, v1, v155, vcc
	v_lshlrev_b32_e32 v237, 2, v237
	ds_bpermute_b32 v238, v237, v235
	s_waitcnt lgkmcnt(1)
	v_max_f32_e32 v236, v236, v236
	v_max_f32_e32 v229, v229, v236
	ds_bpermute_b32 v236, v237, v229
	s_waitcnt lgkmcnt(1)
	v_add_f32_e32 v235, v235, v238
	v_mul_f32_e32 v235, 0x39800000, v235
	v_mul_f32_e32 v237, 0x4f800000, v235
	v_cmp_gt_f32_e32 vcc, s76, v235
	s_waitcnt lgkmcnt(0)
	v_max_f32_e32 v236, v236, v236
	v_max_f32_e32 v229, v229, v236
	v_cndmask_b32_e32 v235, v235, v237, vcc
	v_sqrt_f32_e32 v237, v235
	v_mul_f32_e32 v229, 0x3e088889, v229
	v_add_u32_e32 v236, -1, v237
	v_fma_f32 v238, -v236, v237, v235
	v_cmp_ge_f32_e64 s[88:89], 0, v238
	v_add_u32_e32 v238, 1, v237
	s_nop 0
	v_cndmask_b32_e64 v236, v237, v236, s[88:89]
	v_fma_f32 v237, -v238, v237, v235
	v_cmp_lt_f32_e64 s[88:89], 0, v237
	s_nop 1
	v_cndmask_b32_e64 v236, v236, v238, s[88:89]
	v_mul_f32_e32 v237, 0x37800000, v236
	v_cndmask_b32_e32 v236, v236, v237, vcc
	v_cmp_class_f32_e32 vcc, v235, v233
	s_nop 1
	v_cndmask_b32_e32 v235, v236, v235, vcc
	v_mul_f32_e32 v235, 0x3eab9f56, v235
	v_min_f32_e32 v229, v235, v229
	v_max_f32_e32 v235, 0xda24260, v229
	v_div_scale_f32 v229, s[88:89], v235, v235, 1.0
	v_rcp_f32_e32 v236, v229
	s_nop 0
	v_fma_f32 v237, -v229, v236, 1.0
	v_fmac_f32_e32 v236, v237, v236
	v_div_scale_f32 v237, vcc, 1.0, v235, 1.0
	v_mul_f32_e32 v238, v237, v236
	v_fma_f32 v239, -v229, v238, v237
	v_fmac_f32_e32 v238, v239, v236
	v_fma_f32 v229, -v229, v238, v237
	v_div_fmas_f32 v229, v229, v236, v238
	v_div_fixup_f32 v229, v229, v235, 1.0
	v_mul_f32_e32 v179, v179, v229
	v_mul_f32_e32 v178, v178, v229
	v_floor_f32_e32 v179, v179
	v_mul_f32_e32 v180, v180, v229
	v_floor_f32_e32 v178, v178
	v_add_f32_e32 v179, 0x41000000, v179
	v_floor_f32_e32 v180, v180
	v_add_f32_e32 v178, 0x41000000, v178
	v_med3_f32 v179, v179, 0, v234
	v_add_f32_e32 v180, 0x41000000, v180
	v_med3_f32 v178, v178, 0, v234
	v_cvt_i32_f32_e32 v179, v179
	v_med3_f32 v180, v180, 0, v234
	v_cvt_i32_f32_e32 v178, v178
	v_cvt_i32_f32_sdwa v180, v180 dst_sel:WORD_1 dst_unused:UNUSED_PAD src0_sel:DWORD
	v_lshlrev_b32_e32 v179, 8, v179
	v_mul_f32_e32 v171, v171, v229
	v_mul_f32_e32 v170, v170, v229
	v_or3_b32 v178, v179, v178, v180
	v_mul_f32_e32 v179, v181, v229
	v_mul_f32_e32 v181, v183, v229
	v_floor_f32_e32 v179, v179
	v_mul_f32_e32 v180, v182, v229
	v_floor_f32_e32 v181, v181
	v_mul_f32_e32 v182, v184, v229
	v_add_f32_e32 v179, 0x41000000, v179
	v_floor_f32_e32 v180, v180
	v_add_f32_e32 v181, 0x41000000, v181
	v_floor_f32_e32 v182, v182
	v_mul_f32_e32 v183, v185, v229
	v_floor_f32_e32 v171, v171
	v_mul_f32_e32 v172, v172, v229
	v_med3_f32 v179, v179, 0, v234
	v_add_f32_e32 v180, 0x41000000, v180
	v_med3_f32 v181, v181, 0, v234
	v_add_f32_e32 v182, 0x41000000, v182
	v_floor_f32_e32 v183, v183
	v_floor_f32_e32 v170, v170
	v_add_f32_e32 v171, 0x41000000, v171
	v_floor_f32_e32 v172, v172
	v_mul_f32_e32 v175, v175, v229
	v_cvt_i32_f32_sdwa v179, v179 dst_sel:BYTE_3 dst_unused:UNUSED_PAD src0_sel:DWORD
	v_med3_f32 v180, v180, 0, v234
	v_cvt_i32_f32_e32 v181, v181
	v_med3_f32 v182, v182, 0, v234
	v_add_f32_e32 v183, 0x41000000, v183
	v_add_f32_e32 v170, 0x41000000, v170
	v_med3_f32 v171, v171, 0, v234
	v_add_f32_e32 v172, 0x41000000, v172
	v_mul_f32_e32 v174, v174, v229
	v_floor_f32_e32 v175, v175
	v_mul_f32_e32 v176, v176, v229
	v_cvt_i32_f32_e32 v180, v180
	v_cvt_i32_f32_sdwa v182, v182 dst_sel:WORD_1 dst_unused:UNUSED_PAD src0_sel:DWORD
	v_med3_f32 v183, v183, 0, v234
	v_med3_f32 v170, v170, 0, v234
	v_cvt_i32_f32_e32 v171, v171
	v_med3_f32 v172, v172, 0, v234
	v_floor_f32_e32 v174, v174
	v_add_f32_e32 v175, 0x41000000, v175
	v_floor_f32_e32 v176, v176
	v_cvt_i32_f32_sdwa v183, v183 dst_sel:BYTE_3 dst_unused:UNUSED_PAD src0_sel:DWORD
	v_cvt_i32_f32_e32 v170, v170
	v_cvt_i32_f32_sdwa v172, v172 dst_sel:WORD_1 dst_unused:UNUSED_PAD src0_sel:DWORD
	v_add_f32_e32 v174, 0x41000000, v174
	v_med3_f32 v175, v175, 0, v234
	v_add_f32_e32 v176, 0x41000000, v176
	v_med3_f32 v174, v174, 0, v234
	v_cvt_i32_f32_e32 v175, v175
	v_med3_f32 v176, v176, 0, v234
	v_bitop3_b32 v178, v178, s77, v179 bitop3:0x36
	v_lshlrev_b32_e32 v179, 8, v181
	v_cvt_i32_f32_e32 v174, v174
	v_cvt_i32_f32_sdwa v176, v176 dst_sel:WORD_1 dst_unused:UNUSED_PAD src0_sel:DWORD
	v_or3_b32 v179, v179, v180, v182
	v_lshlrev_b32_e32 v171, 8, v171
	v_or_b32_e32 v180, v179, v183
	v_bitop3_b32 v179, v179, s77, v183 bitop3:0x36
	v_or3_b32 v170, v171, v170, v172
	v_mul_f32_e32 v171, v173, v229
	v_mul_f32_e32 v173, v223, v229
	v_cndmask_b32_e64 v179, v179, v180, s[86:87]
	v_floor_f32_e32 v171, v171
	v_mul_f32_e32 v172, v222, v229
	v_floor_f32_e32 v173, v173
	v_mul_f32_e32 v180, v224, v229
	v_lshlrev_b32_e32 v175, 8, v175
	v_add_f32_e32 v171, 0x41000000, v171
	v_floor_f32_e32 v172, v172
	v_add_f32_e32 v173, 0x41000000, v173
	v_floor_f32_e32 v180, v180
	v_or3_b32 v174, v175, v174, v176
	v_mul_f32_e32 v175, v177, v229
	v_mul_f32_e32 v167, v167, v229
	v_med3_f32 v171, v171, 0, v234
	v_add_f32_e32 v172, 0x41000000, v172
	v_med3_f32 v173, v173, 0, v234
	v_add_f32_e32 v180, 0x41000000, v180
	v_floor_f32_e32 v175, v175
	v_mul_f32_e32 v166, v166, v229
	v_floor_f32_e32 v167, v167
	v_mul_f32_e32 v168, v168, v229
	v_cvt_i32_f32_sdwa v171, v171 dst_sel:BYTE_3 dst_unused:UNUSED_PAD src0_sel:DWORD
	v_med3_f32 v172, v172, 0, v234
	v_cvt_i32_f32_e32 v173, v173
	v_med3_f32 v180, v180, 0, v234
	v_add_f32_e32 v175, 0x41000000, v175
	v_floor_f32_e32 v166, v166
	v_add_f32_e32 v167, 0x41000000, v167
	v_floor_f32_e32 v168, v168
	v_cvt_i32_f32_e32 v172, v172
	v_cvt_i32_f32_sdwa v180, v180 dst_sel:WORD_1 dst_unused:UNUSED_PAD src0_sel:DWORD
	v_med3_f32 v175, v175, 0, v234
	v_add_f32_e32 v166, 0x41000000, v166
	v_med3_f32 v167, v167, 0, v234
	v_add_f32_e32 v168, 0x41000000, v168
	v_cvt_i32_f32_sdwa v175, v175 dst_sel:BYTE_3 dst_unused:UNUSED_PAD src0_sel:DWORD
	v_med3_f32 v166, v166, 0, v234
	v_cvt_i32_f32_e32 v167, v167
	v_med3_f32 v168, v168, 0, v234
	v_cvt_i32_f32_e32 v166, v166
	v_cvt_i32_f32_sdwa v168, v168 dst_sel:WORD_1 dst_unused:UNUSED_PAD src0_sel:DWORD
	v_mul_f32_e32 v181, v225, v229
	v_bitop3_b32 v170, v170, s77, v171 bitop3:0x36
	v_lshlrev_b32_e32 v171, 8, v173
	v_floor_f32_e32 v181, v181
	v_or3_b32 v171, v171, v172, v180
	v_mul_f32_e32 v180, v211, v229
	v_mul_f32_e32 v169, v169, v229
	v_add_f32_e32 v181, 0x41000000, v181
	v_mul_f32_e32 v173, v210, v229
	v_floor_f32_e32 v180, v180
	v_mul_f32_e32 v182, v212, v229
	v_floor_f32_e32 v169, v169
	v_bitop3_b32 v174, v174, s77, v175 bitop3:0x36
	v_lshlrev_b32_e32 v167, 8, v167
	v_mul_f32_e32 v175, v219, v229
	v_med3_f32 v181, v181, 0, v234
	v_floor_f32_e32 v173, v173
	v_add_f32_e32 v180, 0x41000000, v180
	v_floor_f32_e32 v182, v182
	v_add_f32_e32 v169, 0x41000000, v169
	v_or3_b32 v166, v167, v166, v168
	v_mul_f32_e32 v168, v218, v229
	v_floor_f32_e32 v175, v175
	v_mul_f32_e32 v176, v220, v229
	v_cvt_i32_f32_sdwa v181, v181 dst_sel:BYTE_3 dst_unused:UNUSED_PAD src0_sel:DWORD
	v_add_f32_e32 v173, 0x41000000, v173
	v_med3_f32 v180, v180, 0, v234
	v_add_f32_e32 v182, 0x41000000, v182
	v_med3_f32 v169, v169, 0, v234
	v_floor_f32_e32 v168, v168
	v_add_f32_e32 v175, 0x41000000, v175
	v_floor_f32_e32 v176, v176
	v_med3_f32 v173, v173, 0, v234
	v_cvt_i32_f32_e32 v180, v180
	v_med3_f32 v182, v182, 0, v234
	v_cvt_i32_f32_sdwa v169, v169 dst_sel:BYTE_3 dst_unused:UNUSED_PAD src0_sel:DWORD
	v_add_f32_e32 v168, 0x41000000, v168
	v_med3_f32 v175, v175, 0, v234
	v_add_f32_e32 v176, 0x41000000, v176
	v_cvt_i32_f32_e32 v173, v173
	v_cvt_i32_f32_sdwa v182, v182 dst_sel:WORD_1 dst_unused:UNUSED_PAD src0_sel:DWORD
	v_med3_f32 v168, v168, 0, v234
	v_cvt_i32_f32_e32 v175, v175
	v_med3_f32 v176, v176, 0, v234
	v_cvt_i32_f32_e32 v168, v168
	v_cvt_i32_f32_sdwa v176, v176 dst_sel:WORD_1 dst_unused:UNUSED_PAD src0_sel:DWORD
	v_or_b32_e32 v172, v171, v181
	v_bitop3_b32 v171, v171, s77, v181 bitop3:0x36
	v_cndmask_b32_e64 v171, v171, v172, s[86:87]
	v_lshlrev_b32_e32 v172, 8, v180
	v_or_b32_e32 v167, v166, v169
	v_bitop3_b32 v166, v166, s77, v169 bitop3:0x36
	v_or3_b32 v172, v172, v173, v182
	v_mul_f32_e32 v173, v213, v229
	v_mul_f32_e32 v181, v199, v229
	v_cndmask_b32_e64 v166, v166, v167, s[86:87]
	v_lshlrev_b32_e32 v167, 8, v175
	v_floor_f32_e32 v173, v173
	v_mul_f32_e32 v180, v198, v229
	v_floor_f32_e32 v181, v181
	v_mul_f32_e32 v182, v200, v229
	v_or3_b32 v167, v167, v168, v176
	v_mul_f32_e32 v168, v221, v229
	v_mul_f32_e32 v175, v215, v229
	v_add_f32_e32 v173, 0x41000000, v173
	v_floor_f32_e32 v180, v180
	v_add_f32_e32 v181, 0x41000000, v181
	v_floor_f32_e32 v182, v182
	v_mul_f32_e32 v183, v201, v229
	v_floor_f32_e32 v168, v168
	v_mul_f32_e32 v169, v214, v229
	v_floor_f32_e32 v175, v175
	v_mul_f32_e32 v176, v216, v229
	v_med3_f32 v173, v173, 0, v234
	v_add_f32_e32 v180, 0x41000000, v180
	v_med3_f32 v181, v181, 0, v234
	v_add_f32_e32 v182, 0x41000000, v182
	v_floor_f32_e32 v183, v183
	v_add_f32_e32 v168, 0x41000000, v168
	v_floor_f32_e32 v169, v169
	v_add_f32_e32 v175, 0x41000000, v175
	v_floor_f32_e32 v176, v176
	v_cvt_i32_f32_sdwa v173, v173 dst_sel:BYTE_3 dst_unused:UNUSED_PAD src0_sel:DWORD
	v_med3_f32 v180, v180, 0, v234
	v_cvt_i32_f32_e32 v181, v181
	v_med3_f32 v182, v182, 0, v234
	v_add_f32_e32 v183, 0x41000000, v183
	v_med3_f32 v168, v168, 0, v234
	v_add_f32_e32 v169, 0x41000000, v169
	v_med3_f32 v175, v175, 0, v234
	v_add_f32_e32 v176, 0x41000000, v176
	v_cvt_i32_f32_e32 v180, v180
	v_cvt_i32_f32_sdwa v182, v182 dst_sel:WORD_1 dst_unused:UNUSED_PAD src0_sel:DWORD
	v_med3_f32 v183, v183, 0, v234
	v_cvt_i32_f32_sdwa v168, v168 dst_sel:BYTE_3 dst_unused:UNUSED_PAD src0_sel:DWORD
	v_med3_f32 v169, v169, 0, v234
	v_cvt_i32_f32_e32 v175, v175
	v_med3_f32 v176, v176, 0, v234
	v_cvt_i32_f32_sdwa v183, v183 dst_sel:BYTE_3 dst_unused:UNUSED_PAD src0_sel:DWORD
	v_cvt_i32_f32_e32 v169, v169
	v_cvt_i32_f32_sdwa v176, v176 dst_sel:WORD_1 dst_unused:UNUSED_PAD src0_sel:DWORD
	v_bitop3_b32 v172, v172, s77, v173 bitop3:0x36
	v_lshlrev_b32_e32 v173, 8, v181
	v_or3_b32 v173, v173, v180, v182
	v_mul_f32_e32 v177, v217, v229
	v_bitop3_b32 v167, v167, s77, v168 bitop3:0x36
	v_lshlrev_b32_e32 v168, 8, v175
	v_or_b32_e32 v180, v173, v183
	v_bitop3_b32 v173, v173, s77, v183 bitop3:0x36
	v_floor_f32_e32 v177, v177
	v_or3_b32 v168, v168, v169, v176
	v_mul_f32_e32 v176, v203, v229
	v_cndmask_b32_e64 v173, v173, v180, s[86:87]
	v_add_f32_e32 v177, 0x41000000, v177
	v_mul_f32_e32 v175, v202, v229
	v_floor_f32_e32 v176, v176
	v_mul_f32_e32 v180, v204, v229
	v_med3_f32 v177, v177, 0, v234
	v_floor_f32_e32 v175, v175
	v_add_f32_e32 v176, 0x41000000, v176
	v_floor_f32_e32 v180, v180
	v_cvt_i32_f32_sdwa v177, v177 dst_sel:BYTE_3 dst_unused:UNUSED_PAD src0_sel:DWORD
	v_add_f32_e32 v175, 0x41000000, v175
	v_med3_f32 v176, v176, 0, v234
	v_add_f32_e32 v180, 0x41000000, v180
	v_med3_f32 v175, v175, 0, v234
	v_cvt_i32_f32_e32 v176, v176
	v_med3_f32 v180, v180, 0, v234
	v_cvt_i32_f32_e32 v175, v175
	v_cvt_i32_f32_sdwa v180, v180 dst_sel:WORD_1 dst_unused:UNUSED_PAD src0_sel:DWORD
	v_mul_f32_e32 v191, v191, v229
	v_mul_f32_e32 v190, v190, v229
	v_floor_f32_e32 v191, v191
	v_mul_f32_e32 v192, v192, v229
	v_or_b32_e32 v169, v168, v177
	v_bitop3_b32 v168, v168, s77, v177 bitop3:0x36
	v_floor_f32_e32 v190, v190
	v_add_f32_e32 v191, 0x41000000, v191
	v_floor_f32_e32 v192, v192
	v_cndmask_b32_e64 v168, v168, v169, s[86:87]
	v_lshlrev_b32_e32 v169, 8, v176
	v_add_f32_e32 v190, 0x41000000, v190
	v_med3_f32 v191, v191, 0, v234
	v_add_f32_e32 v192, 0x41000000, v192
	v_or3_b32 v169, v169, v175, v180
	v_mul_f32_e32 v175, v205, v229
	v_mul_f32_e32 v177, v195, v229
	v_med3_f32 v190, v190, 0, v234
	v_cvt_i32_f32_e32 v191, v191
	v_med3_f32 v192, v192, 0, v234
	v_floor_f32_e32 v175, v175
	v_mul_f32_e32 v176, v194, v229
	v_floor_f32_e32 v177, v177
	v_mul_f32_e32 v180, v196, v229
	v_mul_f32_e32 v163, v163, v229
	v_cvt_i32_f32_e32 v190, v190
	v_cvt_i32_f32_sdwa v192, v192 dst_sel:WORD_1 dst_unused:UNUSED_PAD src0_sel:DWORD
	v_add_f32_e32 v175, 0x41000000, v175
	v_floor_f32_e32 v176, v176
	v_add_f32_e32 v177, 0x41000000, v177
	v_floor_f32_e32 v180, v180
	v_mul_f32_e32 v181, v197, v229
	v_mul_f32_e32 v162, v162, v229
	v_floor_f32_e32 v163, v163
	v_mul_f32_e32 v164, v164, v229
	v_mul_f32_e32 v207, v207, v229
	v_med3_f32 v175, v175, 0, v234
	v_add_f32_e32 v176, 0x41000000, v176
	v_med3_f32 v177, v177, 0, v234
	v_add_f32_e32 v180, 0x41000000, v180
	v_floor_f32_e32 v181, v181
	v_floor_f32_e32 v162, v162
	v_add_f32_e32 v163, 0x41000000, v163
	v_floor_f32_e32 v164, v164
	v_mul_f32_e32 v165, v165, v229
	v_mul_f32_e32 v206, v206, v229
	v_floor_f32_e32 v207, v207
	v_mul_f32_e32 v208, v208, v229
	v_cvt_i32_f32_sdwa v175, v175 dst_sel:BYTE_3 dst_unused:UNUSED_PAD src0_sel:DWORD
	v_med3_f32 v176, v176, 0, v234
	v_cvt_i32_f32_e32 v177, v177
	v_med3_f32 v180, v180, 0, v234
	v_add_f32_e32 v181, 0x41000000, v181
	v_add_f32_e32 v162, 0x41000000, v162
	v_med3_f32 v163, v163, 0, v234
	v_add_f32_e32 v164, 0x41000000, v164
	v_floor_f32_e32 v165, v165
	v_floor_f32_e32 v206, v206
	v_add_f32_e32 v207, 0x41000000, v207
	v_floor_f32_e32 v208, v208
	v_mul_f32_e32 v209, v209, v229
	v_lshlrev_b32_e32 v191, 8, v191
	v_mul_f32_e32 v187, v187, v229
	v_cvt_i32_f32_e32 v176, v176
	v_cvt_i32_f32_sdwa v180, v180 dst_sel:WORD_1 dst_unused:UNUSED_PAD src0_sel:DWORD
	v_med3_f32 v181, v181, 0, v234
	v_med3_f32 v162, v162, 0, v234
	v_cvt_i32_f32_e32 v163, v163
	v_med3_f32 v164, v164, 0, v234
	v_add_f32_e32 v165, 0x41000000, v165
	v_add_f32_e32 v206, 0x41000000, v206
	v_med3_f32 v207, v207, 0, v234
	v_add_f32_e32 v208, 0x41000000, v208
	v_floor_f32_e32 v209, v209
	v_or3_b32 v190, v191, v190, v192
	v_mul_f32_e32 v191, v193, v229
	v_mul_f32_e32 v186, v186, v229
	v_floor_f32_e32 v187, v187
	v_mul_f32_e32 v188, v188, v229
	v_cvt_i32_f32_sdwa v181, v181 dst_sel:BYTE_3 dst_unused:UNUSED_PAD src0_sel:DWORD
	v_cvt_i32_f32_e32 v162, v162
	v_cvt_i32_f32_sdwa v164, v164 dst_sel:WORD_1 dst_unused:UNUSED_PAD src0_sel:DWORD
	v_med3_f32 v165, v165, 0, v234
	v_med3_f32 v206, v206, 0, v234
	v_cvt_i32_f32_e32 v207, v207
	v_med3_f32 v208, v208, 0, v234
	v_add_f32_e32 v209, 0x41000000, v209
	v_floor_f32_e32 v191, v191
	v_floor_f32_e32 v186, v186
	v_add_f32_e32 v187, 0x41000000, v187
	v_floor_f32_e32 v188, v188
	v_mul_f32_e32 v189, v189, v229
	v_cvt_i32_f32_sdwa v165, v165 dst_sel:BYTE_3 dst_unused:UNUSED_PAD src0_sel:DWORD
	v_cvt_i32_f32_e32 v206, v206
	v_cvt_i32_f32_sdwa v208, v208 dst_sel:WORD_1 dst_unused:UNUSED_PAD src0_sel:DWORD
	v_med3_f32 v209, v209, 0, v234
	v_add_f32_e32 v191, 0x41000000, v191
	v_add_f32_e32 v186, 0x41000000, v186
	v_med3_f32 v187, v187, 0, v234
	v_add_f32_e32 v188, 0x41000000, v188
	v_floor_f32_e32 v189, v189
	v_bitop3_b32 v169, v169, s77, v175 bitop3:0x36
	v_lshlrev_b32_e32 v175, 8, v177
	v_cvt_i32_f32_sdwa v209, v209 dst_sel:BYTE_3 dst_unused:UNUSED_PAD src0_sel:DWORD
	v_med3_f32 v191, v191, 0, v234
	v_med3_f32 v186, v186, 0, v234
	v_cvt_i32_f32_e32 v187, v187
	v_med3_f32 v188, v188, 0, v234
	v_add_f32_e32 v189, 0x41000000, v189
	v_or3_b32 v175, v175, v176, v180
	v_lshlrev_b32_e32 v163, 8, v163
	v_cvt_i32_f32_sdwa v191, v191 dst_sel:BYTE_3 dst_unused:UNUSED_PAD src0_sel:DWORD
	v_cvt_i32_f32_e32 v186, v186
	v_cvt_i32_f32_sdwa v188, v188 dst_sel:WORD_1 dst_unused:UNUSED_PAD src0_sel:DWORD
	v_med3_f32 v189, v189, 0, v234
	v_or_b32_e32 v176, v175, v181
	v_bitop3_b32 v175, v175, s77, v181 bitop3:0x36
	v_or3_b32 v162, v163, v162, v164
	v_lshlrev_b32_e32 v207, 8, v207
	v_cvt_i32_f32_sdwa v189, v189 dst_sel:BYTE_3 dst_unused:UNUSED_PAD src0_sel:DWORD
	v_cndmask_b32_e64 v175, v175, v176, s[86:87]
	v_bitop3_b32 v176, v162, s77, v165 bitop3:0x36
	v_mov_b32_e32 v162, s61
	v_mov_b32_e32 v163, s69
	v_or3_b32 v206, v207, v206, v208
	v_cndmask_b32_e64 v163, v162, v163, s[86:87]
	v_mov_b32_e32 v162, s60
	v_mov_b32_e32 v164, s68
	v_or_b32_e32 v207, v206, v209
	v_bitop3_b32 v206, v206, s77, v209 bitop3:0x36
	v_lshlrev_b32_e32 v187, 8, v187
	v_cndmask_b32_e64 v162, v162, v164, s[86:87]
	v_lshlrev_b64 v[164:165], 8, v[230:231]
	v_cndmask_b32_e64 v206, v206, v207, s[86:87]
	v_bitop3_b32 v190, v190, s77, v191 bitop3:0x36
	v_or3_b32 v186, v187, v186, v188
	v_lshl_add_u64 v[162:163], v[162:163], 0, v[164:165]
	v_mov_b32_e32 v229, v227
	v_or_b32_e32 v187, v186, v189
	v_bitop3_b32 v186, v186, s77, v189 bitop3:0x36
	v_lshl_add_u64 v[162:163], v[162:163], 0, v[228:229]
	v_lshl_or_b32 v164, v190, 4, v206
	v_cndmask_b32_e64 v186, v186, v187, s[86:87]
	global_store_dword v[162:163], v164, off
	v_add_co_u32_e32 v164, vcc, s78, v162
	v_lshl_or_b32 v177, v178, 4, v186
	s_nop 0
	v_addc_co_u32_e32 v165, vcc, 0, v163, vcc
	global_store_dword v[164:165], v177, off
	v_add_co_u32_e32 v164, vcc, s79, v162
	v_lshl_or_b32 v170, v170, 4, v179
	s_nop 0
	v_addc_co_u32_e32 v165, vcc, 0, v163, vcc
	global_store_dword v[164:165], v170, off
	v_add_co_u32_e32 v164, vcc, s80, v162
	v_lshl_or_b32 v170, v172, 4, v171
	s_nop 0
	v_addc_co_u32_e32 v165, vcc, 0, v163, vcc
	global_store_dword v[164:165], v170, off
	v_add_co_u32_e32 v164, vcc, s81, v162
	v_lshl_or_b32 v170, v174, 4, v173
	s_nop 0
	v_addc_co_u32_e32 v165, vcc, 0, v163, vcc
	global_store_dword v[164:165], v170, off
	v_add_co_u32_e32 v164, vcc, 0x1400000, v162
	v_lshl_or_b32 v166, v167, 4, v166
	s_nop 0
	v_addc_co_u32_e32 v165, vcc, 0, v163, vcc
	global_store_dword v[164:165], v166, off
	v_add_co_u32_e32 v164, vcc, 0x1800000, v162
	v_lshl_or_b32 v166, v169, 4, v168
	s_nop 0
	v_addc_co_u32_e32 v165, vcc, 0, v163, vcc
	v_add_co_u32_e32 v162, vcc, 0x1c00000, v162
	global_store_dword v[164:165], v166, off
	v_lshl_or_b32 v164, v176, 4, v175
	v_addc_co_u32_e32 v163, vcc, 0, v163, vcc
	global_store_dword v[162:163], v164, off
	s_and_saveexec_b64 s[88:89], s[82:83]
	s_cbranch_execz .Luvh_skip_scale
	v_mov_b32_e32 v162, s67
	v_mov_b32_e32 v163, s71
	v_cndmask_b32_e64 v163, v162, v163, s[86:87]
	v_mov_b32_e32 v162, s66
	v_mov_b32_e32 v164, s70
	v_cndmask_b32_e64 v162, v162, v164, s[86:87]
	v_lshl_add_u64 v[162:163], v[230:231], 2, v[162:163]
	global_store_dword v[162:163], v235, off
